# MLA MFMA segment PV-first with prefetch before barrier + setprio (MLA M, diff S)
# speedup vs baseline: 1.0433x; 1.0089x over previous
; #define PK4(P, BASE, OUT) do { u32x4 w = {cvtpk(P[BASE + 0], P[BASE + 1]), cvtpk(P[BASE + 2], P[BASE + 3]), cvtpk(P[BASE + 4], P[BASE + 5]), cvtpk(P[BASE + 6], P[BASE + 7])}; \
;     OUT = *reinterpret_cast<bf16x8*>(&w); } while (0)
; __device__ __forceinline__ void smax_tile(f32x16& p0, f32x16& p1, float& mhat, float& l_reg, f32x16 (&o)[4], float* al_l, const bool first, int r32, int hi,
;                                           bf16x8& pa0, bf16x8& pa1, bf16x8& pa2, bf16x8& pa3) {
;     ...
; #pragma unroll
;     for (int r = 0; r < 16; ++r) p0[r] = __builtin_amdgcn_exp2f(p0[r]);
; #pragma unroll
;     for (int r = 0; r < 16; ++r) p1[r] = __builtin_amdgcn_exp2f(p1[r]);
;     float ps = p0[0];
; #pragma unroll
;     for (int r = 1; r < 16; ++r) ps += p0[r];
; #pragma unroll
;     for (int r = 0; r < 16; ++r) ps += p1[r];
;     { auto rr = __builtin_amdgcn_permlane32_swap(__float_as_uint(ps), __float_as_uint(ps), false, false); ps = __uint_as_float(rr[0]) + __uint_as_float(rr[1]); }
;     l_reg += ps;
;     ...
;     PK4(p0, 0, pa0); PK4(p0, 8, pa1); PK4(p1, 0, pa2); PK4(p1, 8, pa3);
.LBB0_605:
	v_exp_f32_e32 v96, v96
	v_exp_f32_e32 v97, v97
	v_exp_f32_e32 v98, v98
	v_exp_f32_e32 v99, v99
	v_exp_f32_e32 v100, v100
	v_exp_f32_e32 v101, v101
	v_add_f32_e32 v160, v96, v97
	v_exp_f32_e32 v102, v102
	v_add_f32_e32 v160, v98, v160
	v_exp_f32_e32 v103, v103
	v_add_f32_e32 v160, v99, v160
	v_exp_f32_e32 v104, v104
	v_add_f32_e32 v160, v100, v160
	v_exp_f32_e32 v105, v105
	v_add_f32_e32 v160, v101, v160
	v_exp_f32_e32 v106, v106
	v_add_f32_e32 v160, v102, v160
	v_exp_f32_e32 v107, v107
	v_add_f32_e32 v160, v103, v160
	v_exp_f32_e32 v108, v108
	v_add_f32_e32 v160, v104, v160
	v_exp_f32_e32 v109, v109
	v_add_f32_e32 v160, v105, v160
	v_exp_f32_e32 v110, v110
	v_add_f32_e32 v160, v106, v160
	v_exp_f32_e32 v111, v111
	v_add_f32_e32 v160, v107, v160
	v_exp_f32_e32 v80, v80
	v_add_f32_e32 v160, v108, v160
	v_exp_f32_e32 v81, v81
	v_add_f32_e32 v160, v109, v160
	v_exp_f32_e32 v82, v82
	v_add_f32_e32 v160, v110, v160
	v_exp_f32_e32 v83, v83
	v_add_f32_e32 v160, v111, v160
	v_exp_f32_e32 v84, v84
	v_add_f32_e32 v160, v80, v160
	v_exp_f32_e32 v85, v85
	v_add_f32_e32 v160, v81, v160
	v_exp_f32_e32 v86, v86
	v_add_f32_e32 v160, v82, v160
	v_exp_f32_e32 v87, v87
	v_add_f32_e32 v160, v83, v160
	v_exp_f32_e32 v88, v88
	v_add_f32_e32 v160, v84, v160
	v_exp_f32_e32 v89, v89
	v_add_f32_e32 v160, v85, v160
	v_exp_f32_e32 v90, v90
	v_add_f32_e32 v160, v86, v160
	v_exp_f32_e32 v91, v91
	v_add_f32_e32 v160, v87, v160
	v_exp_f32_e32 v92, v92
	v_add_f32_e32 v160, v88, v160
	v_exp_f32_e32 v93, v93
	v_add_f32_e32 v160, v89, v160
	v_exp_f32_e32 v94, v94
	v_add_f32_e32 v160, v90, v160
	v_exp_f32_e32 v95, v95
	v_add_f32_e32 v160, v91, v160
	v_add_f32_e32 v160, v92, v160
	v_add_f32_e32 v160, v93, v160
	v_add_f32_e32 v160, v94, v160
	v_add_f32_e32 v160, v95, v160
	v_mov_b32_e32 v161, v160
	s_nop 1
	v_permlane32_swap_b32_e32 v160, v161
	v_add_f32_e32 v160, v160, v161
	v_add_f32_e32 v204, v204, v160
	v_cvt_pk_bf16_f32 v172, v96, v97
	v_cvt_pk_bf16_f32 v173, v98, v99
	v_cvt_pk_bf16_f32 v174, v100, v101
	v_cvt_pk_bf16_f32 v175, v102, v103
	v_cvt_pk_bf16_f32 v168, v104, v105
	v_cvt_pk_bf16_f32 v169, v106, v107
	v_cvt_pk_bf16_f32 v170, v108, v109
	v_cvt_pk_bf16_f32 v171, v110, v111
	v_cvt_pk_bf16_f32 v164, v80, v81
	v_cvt_pk_bf16_f32 v165, v82, v83
	v_cvt_pk_bf16_f32 v166, v84, v85
	v_cvt_pk_bf16_f32 v167, v86, v87
	v_cvt_pk_bf16_f32 v160, v88, v89
	v_cvt_pk_bf16_f32 v161, v90, v91
	v_cvt_pk_bf16_f32 v162, v92, v93
	v_cvt_pk_bf16_f32 v163, v94, v95
	s_mul_i32 s47, s26, 0x6000
	s_addk_i32 s93, 0xc000
	s_cmp_lg_u32 s26, 0
	s_cselect_b32 s46, s93, 0x8000
	v_add_u32_e32 v227, s46, v202
	v_add_u32_e32 v207, s47, v185
	v_add_u32_e32 v224, s47, v187
	v_add_u32_e32 v225, s47, v205
	v_add_u32_e32 v226, s47, v206
	s_waitcnt lgkmcnt(0)
	ds_read_b64_tr_b16 v[208:209], v227 offset:0
	ds_read_b64_tr_b16 v[210:211], v227 offset:2048
	ds_read_b64_tr_b16 v[212:213], v227 offset:512
	ds_read_b64_tr_b16 v[214:215], v227 offset:2560
	ds_read_b64_tr_b16 v[216:217], v227 offset:1024
	ds_read_b64_tr_b16 v[218:219], v227 offset:3072
	ds_read_b64_tr_b16 v[220:221], v227 offset:1536
	ds_read_b64_tr_b16 v[222:223], v227 offset:3584
	s_barrier
; template <int DQK, bool HASQK, bool HASPV, int J>
; __device__ __forceinline__ void slot_read(bf16x8 (&kf)[DQK / 16][2], s16x4 (&vf)[4][8], const int (&ka_)[4], int vb_) {
;     constexpr int NQS = HASQK ? 2 * (DQK / 16) : 0, NS = NQS + (HASPV ? 16 : 0);
;     if constexpr (J < NQS) { constexpr int d0 = J >> 1, h = J & 1; dsr128<(d0 >> 2) * 128 + h * 32 * DQK * 2>(kf[d0][h], ka_[d0 & 3]); }
;     else if constexpr (J < NS) { constexpr int q = J - NQS, g = q >> 2, d = q & 3; dstr64<v_rd_off(d, g, 0)>(vf[g][2 * d], vb_); dstr64<v_rd_off(d, g, 1)>(vf[g][2 * d + 1], vb_); }
; }
; template <int DQK, bool HASQK, bool HASPV, int J> ...
;     constexpr int NQS = HASQK ? 2 * (DQK / 16) : 0, NS = NQS + (HASPV ? 16 : 0);
;     if constexpr (J < NS) {
;         constexpr int rd1 = (J + 1 < NS) ? ((J + 1 < NQS) ? 1 : 2) : 0, rd2 = (J + 2 < NS) ? ((J + 2 < NQS) ? 1 : 2) : 0, rd3 = (J + 3 < NS) ? ((J + 3 < NQS) ? 1 : 2) : 0, NW = rd1 + rd2 + rd3;
;     ...
;         if constexpr (J < NQS) { constexpr int d0 = J >> 1, h = J & 1;
;             LWN1(kf[d0][h]); SBAR();
;             if constexpr (h == 0) p0 = __builtin_amdgcn_mfma_f32_32x32x16_bf16(kf[d0][0], qr[d0], (d0 == 0) ? negm : p0, 0, 0, 0);
;             else p1 = __builtin_amdgcn_mfma_f32_32x32x16_bf16(kf[d0][1], qr[d0], (d0 == 0) ? negm : p1, 0, 0, 0);
;         } else { constexpr int q = J - NQS, g = q >> 2, d = q & 3;
;             LWN2(vf[g][2 * d], vf[g][2 * d + 1]); SBAR();
;             o[d] = __builtin_amdgcn_mfma_f32_32x32x16_bf16(pa[g], (bf16x8){vf[g][2 * d][0], vf[g][2 * d][1], vf[g][2 * d][2], vf[g][2 * d][3], vf[g][2 * d + 1][0], vf[g][2 * d + 1][1], vf[g][2 * d + 1][2], vf[g][2 * d + 1][3]}, o[d], 0, 0, 0);
;         }
;     ...
;         SBAR();
;         slot_read<DQK, HASQK, HASPV, J + 4>(kf, vf, ka_, vb_);
;         SBAR();
;         slot_run<DQK, HASQK, HASPV, J + 1>(kf, vf, ka_, vb_, qr, p0, p1, negm, o, pa);
;     }
; }
;     ...
;     for (int i = 0; i < NT - 1; ++i) {
;         SEG_S(i);
;         { const int cp = (ci == 0) ? 2 : ci - 1, cn = (ci == 2) ? 0 : ci + 1;
;           if (DMA_M) { if (i + 3 < NT) DMA_K(i + 3, cp); if (i + 2 < NT) DMA_V(i + 2, cn); }
;           SEG_M(true, true, ci, cp);
;           if (DMA_M && i + 3 < NT) asm volatile("s_waitcnt vmcnt(%0)" :: "n"(NKW + 2) : "memory");
;           else asm volatile("s_waitcnt vmcnt(0)" ::: "memory");
;           BAR_ALL(); }
	s_setprio 1
	s_waitcnt lgkmcnt(6)
	v_mfma_f32_32x32x16_bf16 v[64:79], v[172:175], v[208:211], v[64:79]
	ds_read_b64_tr_b16 v[208:209], v227 offset:4096
	ds_read_b64_tr_b16 v[210:211], v227 offset:6144
	s_waitcnt lgkmcnt(6)
	v_mfma_f32_32x32x16_bf16 v[48:63], v[172:175], v[212:215], v[48:63]
	ds_read_b64_tr_b16 v[212:213], v227 offset:4608
	ds_read_b64_tr_b16 v[214:215], v227 offset:6656
	s_waitcnt lgkmcnt(6)
	v_mfma_f32_32x32x16_bf16 v[32:47], v[172:175], v[216:219], v[32:47]
	ds_read_b64_tr_b16 v[216:217], v227 offset:5120
	ds_read_b64_tr_b16 v[218:219], v227 offset:7168
	s_waitcnt lgkmcnt(6)
	v_mfma_f32_32x32x16_bf16 v[16:31], v[172:175], v[220:223], v[16:31]
	ds_read_b64_tr_b16 v[220:221], v227 offset:5632
	ds_read_b64_tr_b16 v[222:223], v227 offset:7680
	s_waitcnt lgkmcnt(6)
	v_mfma_f32_32x32x16_bf16 v[64:79], v[168:171], v[208:211], v[64:79]
	ds_read_b64_tr_b16 v[208:209], v227 offset:8192
	ds_read_b64_tr_b16 v[210:211], v227 offset:10240
	s_waitcnt lgkmcnt(6)
	v_mfma_f32_32x32x16_bf16 v[48:63], v[168:171], v[212:215], v[48:63]
	ds_read_b64_tr_b16 v[212:213], v227 offset:8704
	ds_read_b64_tr_b16 v[214:215], v227 offset:10752
	s_waitcnt lgkmcnt(6)
	v_mfma_f32_32x32x16_bf16 v[32:47], v[168:171], v[216:219], v[32:47]
	ds_read_b64_tr_b16 v[216:217], v227 offset:9216
	ds_read_b64_tr_b16 v[218:219], v227 offset:11264
	s_waitcnt lgkmcnt(6)
	v_mfma_f32_32x32x16_bf16 v[16:31], v[168:171], v[220:223], v[16:31]
	ds_read_b64_tr_b16 v[220:221], v227 offset:9728
	ds_read_b64_tr_b16 v[222:223], v227 offset:11776
	s_waitcnt lgkmcnt(6)
	v_mfma_f32_32x32x16_bf16 v[64:79], v[164:167], v[208:211], v[64:79]
	ds_read_b64_tr_b16 v[208:209], v227 offset:12288
	ds_read_b64_tr_b16 v[210:211], v227 offset:14336
	s_waitcnt lgkmcnt(6)
	v_mfma_f32_32x32x16_bf16 v[48:63], v[164:167], v[212:215], v[48:63]
	ds_read_b64_tr_b16 v[212:213], v227 offset:12800
	ds_read_b64_tr_b16 v[214:215], v227 offset:14848
	s_waitcnt lgkmcnt(6)
	v_mfma_f32_32x32x16_bf16 v[32:47], v[164:167], v[216:219], v[32:47]
	ds_read_b64_tr_b16 v[216:217], v227 offset:13312
	ds_read_b64_tr_b16 v[218:219], v227 offset:15360
	s_waitcnt lgkmcnt(6)
	v_mfma_f32_32x32x16_bf16 v[16:31], v[164:167], v[220:223], v[16:31]
	ds_read_b64_tr_b16 v[220:221], v227 offset:13824
	ds_read_b64_tr_b16 v[222:223], v227 offset:15872
	v_xor_b32_e32 v80, 0x80000000, v203
	v_mov_b32_e32 v81, v80
	v_mov_b32_e32 v82, v80
	v_mov_b32_e32 v83, v80
	v_mov_b32_e32 v84, v80
	v_mov_b32_e32 v85, v80
	v_mov_b32_e32 v86, v80
	v_mov_b32_e32 v87, v80
	v_mov_b32_e32 v88, v80
	v_mov_b32_e32 v89, v80
	v_mov_b32_e32 v90, v80
	v_mov_b32_e32 v91, v80
	v_mov_b32_e32 v92, v80
	v_mov_b32_e32 v93, v80
	v_mov_b32_e32 v94, v80
	v_mov_b32_e32 v95, v80
	s_waitcnt lgkmcnt(6)
	v_mfma_f32_32x32x16_bf16 v[64:79], v[160:163], v[208:211], v[64:79]
	ds_read_b128 v[208:211], v207 offset:0
	s_waitcnt lgkmcnt(5)
	v_mfma_f32_32x32x16_bf16 v[48:63], v[160:163], v[212:215], v[48:63]
	ds_read_b128 v[212:215], v207 offset:12288
	s_waitcnt lgkmcnt(4)
	v_mfma_f32_32x32x16_bf16 v[32:47], v[160:163], v[216:219], v[32:47]
	ds_read_b128 v[216:219], v224 offset:0
	s_waitcnt lgkmcnt(3)
	v_mfma_f32_32x32x16_bf16 v[16:31], v[160:163], v[220:223], v[16:31]
	ds_read_b128 v[220:223], v224 offset:12288
	s_waitcnt lgkmcnt(3)
	v_mfma_f32_32x32x16_bf16 v[96:111], v[208:211], v[112:115], v[80:95]
	ds_read_b128 v[208:211], v225 offset:0
	s_waitcnt lgkmcnt(3)
	v_mfma_f32_32x32x16_bf16 v[80:95], v[212:215], v[112:115], v[80:95]
	ds_read_b128 v[212:215], v225 offset:12288
	s_waitcnt lgkmcnt(3)
	v_mfma_f32_32x32x16_bf16 v[96:111], v[216:219], v[116:119], v[96:111]
	ds_read_b128 v[216:219], v226 offset:0
	s_waitcnt lgkmcnt(3)
	v_mfma_f32_32x32x16_bf16 v[80:95], v[220:223], v[116:119], v[80:95]
	ds_read_b128 v[220:223], v226 offset:12288
	s_waitcnt lgkmcnt(3)
	v_mfma_f32_32x32x16_bf16 v[96:111], v[208:211], v[120:123], v[96:111]
	ds_read_b128 v[208:211], v207 offset:128
	s_waitcnt lgkmcnt(3)
	v_mfma_f32_32x32x16_bf16 v[80:95], v[212:215], v[120:123], v[80:95]
	ds_read_b128 v[212:215], v207 offset:12416
	s_waitcnt lgkmcnt(3)
	v_mfma_f32_32x32x16_bf16 v[96:111], v[216:219], v[124:127], v[96:111]
	ds_read_b128 v[216:219], v224 offset:128
	s_waitcnt lgkmcnt(3)
	v_mfma_f32_32x32x16_bf16 v[80:95], v[220:223], v[124:127], v[80:95]
	ds_read_b128 v[220:223], v224 offset:12416
	s_waitcnt lgkmcnt(3)
	v_mfma_f32_32x32x16_bf16 v[96:111], v[208:211], v[128:131], v[96:111]
	ds_read_b128 v[208:211], v225 offset:128
	s_waitcnt lgkmcnt(3)
	v_mfma_f32_32x32x16_bf16 v[80:95], v[212:215], v[128:131], v[80:95]
	ds_read_b128 v[212:215], v225 offset:12416
	s_waitcnt lgkmcnt(3)
	v_mfma_f32_32x32x16_bf16 v[96:111], v[216:219], v[132:135], v[96:111]
	ds_read_b128 v[216:219], v226 offset:128
	s_waitcnt lgkmcnt(3)
	v_mfma_f32_32x32x16_bf16 v[80:95], v[220:223], v[132:135], v[80:95]
	ds_read_b128 v[220:223], v226 offset:12416
	s_waitcnt lgkmcnt(3)
	v_mfma_f32_32x32x16_bf16 v[96:111], v[208:211], v[136:139], v[96:111]
	ds_read_b128 v[208:211], v207 offset:256
	s_waitcnt lgkmcnt(3)
	v_mfma_f32_32x32x16_bf16 v[80:95], v[212:215], v[136:139], v[80:95]
	ds_read_b128 v[212:215], v207 offset:12544
	s_waitcnt lgkmcnt(3)
	v_mfma_f32_32x32x16_bf16 v[96:111], v[216:219], v[140:143], v[96:111]
	ds_read_b128 v[216:219], v224 offset:256
	s_waitcnt lgkmcnt(3)
	v_mfma_f32_32x32x16_bf16 v[80:95], v[220:223], v[140:143], v[80:95]
	ds_read_b128 v[220:223], v224 offset:12544
	s_waitcnt lgkmcnt(3)
	v_mfma_f32_32x32x16_bf16 v[96:111], v[208:211], v[144:147], v[96:111]
	ds_read_b128 v[208:211], v225 offset:256
	s_waitcnt lgkmcnt(3)
	v_mfma_f32_32x32x16_bf16 v[80:95], v[212:215], v[144:147], v[80:95]
	ds_read_b128 v[212:215], v225 offset:12544
	s_waitcnt lgkmcnt(3)
	v_mfma_f32_32x32x16_bf16 v[96:111], v[216:219], v[148:151], v[96:111]
	ds_read_b128 v[216:219], v226 offset:256
	s_waitcnt lgkmcnt(3)
	v_mfma_f32_32x32x16_bf16 v[80:95], v[220:223], v[148:151], v[80:95]
	ds_read_b128 v[220:223], v226 offset:12544
	s_waitcnt lgkmcnt(3)
	v_mfma_f32_32x32x16_bf16 v[96:111], v[208:211], v[152:155], v[96:111]
	s_waitcnt lgkmcnt(2)
	v_mfma_f32_32x32x16_bf16 v[80:95], v[212:215], v[152:155], v[80:95]
	s_waitcnt lgkmcnt(1)
	v_mfma_f32_32x32x16_bf16 v[96:111], v[216:219], v[156:159], v[96:111]
	s_waitcnt lgkmcnt(0)
	v_mfma_f32_32x32x16_bf16 v[80:95], v[220:223], v[156:159], v[80:95]
	s_setprio 0
	s_waitcnt vmcnt(0)
	s_waitcnt lgkmcnt(0)
	s_barrier
	s_add_u32 s44, s44, 0x18000
	s_addc_u32 s45, s45, 0
	v_lshl_add_u64 v[194:195], v[194:195], 0, s[28:29]
	s_cmp_eq_u32 s44, 0xbe8000
	v_lshl_add_u64 v[196:197], v[196:197], 0, s[28:29]
	s_cbranch_scc1 .LBB0_616
